# NA attention tile loops: Q-fragment wait moved to the loop top so the QK^T block no longer waits for the next tile's just-issued global loads (merged vmcnt(5..0) -> lgkmcnt only)
# speedup vs baseline: 1.0052x; 1.0020x over previous
.LBB0_713:
	s_waitcnt vmcnt(0)
	s_add_i32 s85, s86, 1
	s_cmp_lt_i32 s85, s64
	s_cselect_b64 s[44:45], -1, 0
	s_cmp_ge_i32 s85, s64
	s_cbranch_scc1 .LBB0_715
	s_cmp_gt_u32 s86, 2
	s_cselect_b32 s46, s65, 33
	s_add_i32 s46, s46, s86
	s_lshl_b32 s46, s46, 6
	v_or_b32_e32 v4, s46, v218
	v_ashrrev_i32_e32 v5, 31, v4
	v_or_b32_e32 v6, s46, v199
	v_lshlrev_b64 v[4:5], 8, v[4:5]
	v_ashrrev_i32_e32 v7, 31, v6
	v_lshl_add_u64 v[4:5], v[192:193], 0, v[4:5]
	v_lshlrev_b64 v[6:7], 8, v[6:7]
	s_ashr_i32 s47, s46, 31
	v_lshl_add_u64 v[6:7], v[192:193], 0, v[6:7]
	global_load_dwordx4 v[124:127], v[4:5], off
	global_load_dwordx4 v[132:135], v[6:7], off
	v_lshl_add_u64 v[4:5], s[46:47], 1, v[190:191]
	v_lshl_add_u64 v[6:7], v[4:5], 0, v[176:177]
	v_lshl_add_u64 v[4:5], v[4:5], 0, v[178:179]
	global_load_dwordx4 v[156:159], v[6:7], off
	global_load_dwordx4 v[160:163], v[4:5], off

.LBB0_717:
	s_andn2_b64 vcc, exec, s[48:49]
	s_cbranch_vccnz .LBB0_757
	s_bitcmp1_b32 s86, 0
	s_cselect_b32 s48, 0x8c00, 0
	s_add_i32 s86, s48, 0
	v_add3_u32 v2, s86, v194, v168
	ds_read_b128 v[4:7], v2
	ds_read_b128 v[8:11], v2 offset:32
	s_mov_b64 s[48:49], -1
	s_andn2_b64 vcc, exec, s[46:47]
	s_waitcnt lgkmcnt(1)
	v_mfma_f32_32x32x16_bf16 v[100:115], v[4:7], v[116:119], 0
	s_waitcnt lgkmcnt(0)
	v_mfma_f32_32x32x16_bf16 v[100:115], v[8:11], v[120:123], v[100:115]
	ds_read_b128 v[4:7], v2 offset:64
	ds_read_b128 v[8:11], v2 offset:96
	s_waitcnt lgkmcnt(1)
	v_mfma_f32_32x32x16_bf16 v[100:115], v[4:7], v[128:131], v[100:115]
	s_waitcnt lgkmcnt(0)
	v_mfma_f32_32x32x16_bf16 v[100:115], v[8:11], v[136:139], v[100:115]
	ds_read_b128 v[4:7], v2 offset:128
	ds_read_b128 v[8:11], v2 offset:160
	s_waitcnt lgkmcnt(1)
	v_mfma_f32_32x32x16_bf16 v[100:115], v[4:7], v[140:143], v[100:115]
	s_waitcnt lgkmcnt(0)
	v_mfma_f32_32x32x16_bf16 v[100:115], v[8:11], v[144:147], v[100:115]
	ds_read_b128 v[4:7], v2 offset:192
	ds_read_b128 v[8:11], v2 offset:224
	v_max_f32_e32 v2, v83, v83
	s_waitcnt lgkmcnt(1)
	v_mfma_f32_32x32x16_bf16 v[100:115], v[4:7], v[148:151], v[100:115]
	s_waitcnt lgkmcnt(0)
	v_mfma_f32_32x32x16_bf16 v[100:115], v[8:11], v[152:155], v[100:115]
	s_cbranch_vccnz .LBB0_720
	s_nop 10
	v_max3_f32 v4, v100, s58, v101
	v_max3_f32 v4, v4, v102, v103
	v_max3_f32 v4, v4, v104, v105
	v_max3_f32 v4, v4, v106, v107
	v_max3_f32 v4, v4, v108, v109
	v_max3_f32 v4, v4, v110, v111
	v_max3_f32 v4, v4, v112, v113
	v_max3_f32 v4, v4, v114, v115
	v_mov_b32_e32 v5, v4
	s_nop 1
	v_permlane32_swap_b32_e32 v4, v5
	v_mul_f32_e32 v4, 0x3e0293ee, v4
	v_max_f32_e32 v4, v2, v4
	v_fma_f32 v5, v100, s59, -v4
	v_exp_f32_e32 v84, v5
	v_fma_f32 v5, v101, s59, -v4
	v_exp_f32_e32 v85, v5
	v_fma_f32 v5, v102, s59, -v4
	v_exp_f32_e32 v86, v5
	v_fma_f32 v6, v103, s59, -v4
	v_exp_f32_e32 v87, v6
	v_fma_f32 v6, v104, s59, -v4
	v_add_f32_e32 v5, 0, v84
	v_exp_f32_e32 v88, v6
	v_fma_f32 v6, v105, s59, -v4
	v_add_f32_e32 v5, v85, v5
	v_exp_f32_e32 v89, v6
	v_fma_f32 v6, v106, s59, -v4
	v_add_f32_e32 v5, v86, v5
	v_exp_f32_e32 v90, v6
	v_fma_f32 v6, v107, s59, -v4
	v_add_f32_e32 v5, v87, v5
	v_exp_f32_e32 v91, v6
	v_fma_f32 v6, v108, s59, -v4
	v_add_f32_e32 v5, v88, v5
	v_exp_f32_e32 v92, v6
	v_fma_f32 v6, v109, s59, -v4
	v_add_f32_e32 v5, v89, v5
	v_exp_f32_e32 v93, v6
	v_fma_f32 v6, v110, s59, -v4
	v_add_f32_e32 v5, v90, v5
	v_exp_f32_e32 v94, v6
	v_fma_f32 v6, v111, s59, -v4
	v_add_f32_e32 v5, v91, v5
	v_exp_f32_e32 v95, v6
	v_fma_f32 v6, v112, s59, -v4
	v_add_f32_e32 v5, v92, v5
	v_exp_f32_e32 v96, v6
	v_fma_f32 v6, v113, s59, -v4
	v_add_f32_e32 v5, v93, v5
	v_exp_f32_e32 v97, v6
	v_fma_f32 v6, v114, s59, -v4
	v_add_f32_e32 v5, v94, v5
	v_exp_f32_e32 v98, v6
	v_add_f32_e32 v5, v95, v5
	v_add_f32_e32 v5, v96, v5
	v_add_f32_e32 v5, v97, v5
	v_add_f32_e32 v6, v98, v5
	v_fma_f32 v5, v115, s59, -v4
	s_mov_b64 s[48:49], 0

.LBB0_2896:
	s_waitcnt vmcnt(0)
	s_add_i32 s85, s86, 1
	s_cmp_lt_i32 s85, s69
	s_cselect_b64 s[48:49], -1, 0
	s_cmp_ge_i32 s85, s69
	s_cbranch_scc1 .LBB0_2898
	s_cmp_gt_u32 s86, 2
	s_cselect_b32 s50, s70, 33
	s_add_i32 s50, s50, s86
	s_lshl_b32 s50, s50, 6
	v_or_b32_e32 v4, s50, v218
	v_ashrrev_i32_e32 v5, 31, v4
	v_or_b32_e32 v6, s50, v171
	v_lshlrev_b64 v[4:5], 8, v[4:5]
	v_ashrrev_i32_e32 v7, 31, v6
	v_lshl_add_u64 v[4:5], v[192:193], 0, v[4:5]
	v_lshlrev_b64 v[6:7], 8, v[6:7]
	s_ashr_i32 s51, s50, 31
	v_lshl_add_u64 v[6:7], v[192:193], 0, v[6:7]
	global_load_dwordx4 v[124:127], v[4:5], off
	global_load_dwordx4 v[132:135], v[6:7], off
	v_lshl_add_u64 v[4:5], s[50:51], 1, v[190:191]
	v_lshl_add_u64 v[6:7], v[4:5], 0, v[182:183]
	v_lshl_add_u64 v[4:5], v[4:5], 0, v[184:185]
	global_load_dwordx4 v[156:159], v[6:7], off
	global_load_dwordx4 v[160:163], v[4:5], off

.LBB0_2900:
	s_andn2_b64 vcc, exec, s[54:55]
	s_cbranch_vccnz .LBB0_2940
	s_bitcmp1_b32 s86, 0
	s_cselect_b32 s54, 0x8c00, 0
	s_add_i32 s86, s54, 0
	v_add3_u32 v2, s86, v197, v170
	ds_read_b128 v[4:7], v2
	ds_read_b128 v[8:11], v2 offset:32
	s_mov_b64 s[54:55], -1
	s_andn2_b64 vcc, exec, s[50:51]
	s_waitcnt lgkmcnt(1)
	v_mfma_f32_32x32x16_bf16 v[100:115], v[4:7], v[116:119], 0
	s_waitcnt lgkmcnt(0)
	v_mfma_f32_32x32x16_bf16 v[100:115], v[8:11], v[120:123], v[100:115]
	ds_read_b128 v[4:7], v2 offset:64
	ds_read_b128 v[8:11], v2 offset:96
	s_waitcnt lgkmcnt(1)
	v_mfma_f32_32x32x16_bf16 v[100:115], v[4:7], v[128:131], v[100:115]
	s_waitcnt lgkmcnt(0)
	v_mfma_f32_32x32x16_bf16 v[100:115], v[8:11], v[136:139], v[100:115]
	ds_read_b128 v[4:7], v2 offset:128
	ds_read_b128 v[8:11], v2 offset:160
	s_waitcnt lgkmcnt(1)
	v_mfma_f32_32x32x16_bf16 v[100:115], v[4:7], v[140:143], v[100:115]
	s_waitcnt lgkmcnt(0)
	v_mfma_f32_32x32x16_bf16 v[100:115], v[8:11], v[144:147], v[100:115]
	ds_read_b128 v[4:7], v2 offset:192
	ds_read_b128 v[8:11], v2 offset:224
	v_max_f32_e32 v2, v83, v83
	s_waitcnt lgkmcnt(1)
	v_mfma_f32_32x32x16_bf16 v[100:115], v[4:7], v[148:151], v[100:115]
	s_waitcnt lgkmcnt(0)
	v_mfma_f32_32x32x16_bf16 v[100:115], v[8:11], v[152:155], v[100:115]
	s_cbranch_vccnz .LBB0_2903
	s_nop 10
	v_max3_f32 v4, v100, s62, v101
	v_max3_f32 v4, v4, v102, v103
	v_max3_f32 v4, v4, v104, v105
	v_max3_f32 v4, v4, v106, v107
	v_max3_f32 v4, v4, v108, v109
	v_max3_f32 v4, v4, v110, v111
	v_max3_f32 v4, v4, v112, v113
	v_max3_f32 v4, v4, v114, v115
	v_mov_b32_e32 v5, v4
	s_nop 1
	v_permlane32_swap_b32_e32 v4, v5
	v_mul_f32_e32 v4, 0x3e0293ee, v4
	v_max_f32_e32 v4, v2, v4
	v_fma_f32 v5, v100, s63, -v4
	v_exp_f32_e32 v84, v5
	v_fma_f32 v5, v101, s63, -v4
	v_exp_f32_e32 v85, v5
	v_fma_f32 v5, v102, s63, -v4
	v_exp_f32_e32 v86, v5
	v_fma_f32 v6, v103, s63, -v4
	v_exp_f32_e32 v87, v6
	v_fma_f32 v6, v104, s63, -v4
	v_add_f32_e32 v5, 0, v84
	v_exp_f32_e32 v88, v6
	v_fma_f32 v6, v105, s63, -v4
	v_add_f32_e32 v5, v85, v5
	v_exp_f32_e32 v89, v6
	v_fma_f32 v6, v106, s63, -v4
	v_add_f32_e32 v5, v86, v5
	v_exp_f32_e32 v90, v6
	v_fma_f32 v6, v107, s63, -v4
	v_add_f32_e32 v5, v87, v5
	v_exp_f32_e32 v91, v6
	v_fma_f32 v6, v108, s63, -v4
	v_add_f32_e32 v5, v88, v5
	v_exp_f32_e32 v92, v6
	v_fma_f32 v6, v109, s63, -v4
	v_add_f32_e32 v5, v89, v5
	v_exp_f32_e32 v93, v6
	v_fma_f32 v6, v110, s63, -v4
	v_add_f32_e32 v5, v90, v5
	v_exp_f32_e32 v94, v6
	v_fma_f32 v6, v111, s63, -v4
	v_add_f32_e32 v5, v91, v5
	v_exp_f32_e32 v95, v6
	v_fma_f32 v6, v112, s63, -v4
	v_add_f32_e32 v5, v92, v5
	v_exp_f32_e32 v96, v6
	v_fma_f32 v6, v113, s63, -v4
	v_add_f32_e32 v5, v93, v5
	v_exp_f32_e32 v97, v6
	v_fma_f32 v6, v114, s63, -v4
	v_add_f32_e32 v5, v94, v5
	v_exp_f32_e32 v98, v6
	v_add_f32_e32 v5, v95, v5
	v_add_f32_e32 v5, v96, v5
	v_add_f32_e32 v5, v97, v5
	v_add_f32_e32 v6, v98, v5
	v_fma_f32 v5, v115, s63, -v4
	s_mov_b64 s[54:55], 0
